# speedup vs baseline: 1.0028x; 1.0017x over previous
.LBB4_2:
	s_or_b64 exec, exec, s[6:7]
	s_load_dwordx2 s[6:7], s[0:1], 0x40
	s_waitcnt vmcnt(10)
	v_lshl_or_b32 v34, v40, 4, v59
	v_ashrrev_i32_e32 v35, 31, v34
	v_lshl_add_u64 v[34:35], v[34:35], 2, s[10:11]
	global_load_dword v96, v[34:35], off offset:12
	global_load_dword v97, v[34:35], off offset:28
	global_load_dword v98, v[34:35], off offset:44
	v_min_i32_e32 v60, 16, v57
	v_lshlrev_b32_e32 v0, 2, v0
	v_lshl_add_u64 v[50:51], s[16:17], 0, v[0:1]
	v_cmp_le_i32_e64 s[0:1], v59, v60
	v_mov_b32_e32 v46, v1
	v_mov_b32_e32 v47, v1
	v_mov_b32_e32 v48, v1
	v_mov_b32_e32 v49, v1
	v_mbcnt_lo_u32_b32 v1, -1, 0
	s_and_saveexec_b64 s[14:15], s[0:1]
	s_cbranch_execz .LBB4_27
	v_mbcnt_hi_u32_b32 v34, -1, v1
	v_and_b32_e32 v35, 0x70, v34
	s_waitcnt lgkmcnt(0)
	s_cmp_gt_i32 s26, 0
	v_lshlrev_b32_e32 v62, 2, v35
	s_cselect_b64 s[16:17], -1, 0
	v_lshlrev_b32_e32 v34, 2, v34
	s_movk_i32 s0, 0x1c0
	s_add_u32 s18, s12, 4
	v_lshlrev_b32_e32 v61, 4, v40
	v_or_b32_e32 v63, 4, v62
	v_or_b32_e32 v64, 8, v62
	v_or_b32_e32 v65, 12, v62
	v_and_or_b32 v66, v34, s0, 16
	s_addc_u32 s19, s13, 0
	v_mov_b32_e32 v46, 0
	s_mov_b64 s[20:21], 0
	s_mov_b32 s27, 0x800000
	v_mov_b32_e32 v67, 0x3ab69700
	s_mov_b32 s28, 0x43000000
	s_mov_b32 s29, 0xc1880000
	v_mov_b32_e32 v68, 0x7f000000
	v_mov_b32_e32 v69, v59
	v_mov_b32_e32 v47, 0
	v_mov_b32_e32 v48, 0
	v_mov_b32_e32 v49, 0
	s_mov_b32 s40, 0
	s_branch .LBB4_5
.LBB4_4:
	s_or_b64 exec, exec, s[4:5]
	s_add_i32 s40, s40, 1
	v_add_u32_e32 v69, 4, v69
	v_cmp_gt_i32_e64 s[0:1], v69, v60
	v_fmac_f32_e32 v46, v52, v36
	v_fmac_f32_e32 v47, v52, v37
	v_fmac_f32_e32 v48, v52, v34
	s_or_b64 s[20:21], s[0:1], s[20:21]
	v_fmac_f32_e32 v49, v52, v35
	s_andn2_b64 exec, exec, s[20:21]
	s_cbranch_execz .LBB4_26
.LBB4_5:
	v_cmp_ne_u32_e64 s[0:1], v69, v59
	s_waitcnt vmcnt(0)
	v_mov_b32_e32 v54, v73
	s_cmp_eq_u32 s40, 0
	s_cbranch_scc1 .Lgc_have
	v_mov_b32_e32 v54, v96
	s_cmp_eq_u32 s40, 1
	s_cbranch_scc1 .Lgc_have
	v_mov_b32_e32 v54, v97
	s_cmp_eq_u32 s40, 2
	s_cbranch_scc1 .Lgc_have
	v_mov_b32_e32 v54, v98
	s_cmp_eq_u32 s40, 3
	s_cbranch_scc1 .Lgc_have
	s_and_saveexec_b64 s[4:5], s[0:1]
	s_cbranch_execz .LBB4_7
	v_add_u32_e32 v34, v69, v61
	v_ashrrev_i32_e32 v35, 31, v34
	v_lshl_add_u64 v[34:35], v[34:35], 2, s[10:11]
	global_load_dword v54, v[34:35], off offset:-4

.Lgc_have:
	v_ashrrev_i32_e32 v55, 31, v54
	v_lshl_add_u64 v[34:35], v[54:55], 2, s[8:9]
	global_load_dword v70, v[34:35], off
	v_lshl_or_b32 v34, v54, 4, v58
	v_ashrrev_i32_e32 v35, 31, v34
	v_lshl_add_u64 v[34:35], v[34:35], 2, s[10:11]
	global_load_dword v52, v[34:35], off
	v_lshlrev_b64 v[34:35], 8, v[54:55]
	v_lshl_add_u64 v[34:35], v[50:51], 0, v[34:35]
	global_load_dwordx4 v[34:37], v[34:35], off
	v_mov_b32_e32 v53, 0
	s_waitcnt vmcnt(2)
	v_cmp_gt_i32_e64 s[0:1], v70, v58
	s_and_saveexec_b64 s[22:23], s[0:1]
	s_cbranch_execz .LBB4_9
	s_waitcnt vmcnt(1)
	v_ashrrev_i32_e32 v53, 31, v52
	v_lshl_add_u64 v[74:75], v[52:53], 2, s[8:9]
	global_load_dword v53, v[74:75], off

	.amdhsa_kernel _Z10gcn_kernelPKiS0_S0_S0_PKfS2_S2_S2_Pf
		.amdhsa_group_segment_fixed_size 26624
		.amdhsa_private_segment_fixed_size 0
		.amdhsa_kernarg_size 72
		.amdhsa_user_sgpr_count 2
		.amdhsa_user_sgpr_dispatch_ptr 0
		.amdhsa_user_sgpr_queue_ptr 0
		.amdhsa_user_sgpr_kernarg_segment_ptr 1
		.amdhsa_user_sgpr_dispatch_id 0
		.amdhsa_user_sgpr_kernarg_preload_length 0
		.amdhsa_user_sgpr_kernarg_preload_offset 0
		.amdhsa_user_sgpr_private_segment_size 0
		.amdhsa_uses_dynamic_stack 0
		.amdhsa_enable_private_segment 0
		.amdhsa_system_sgpr_workgroup_id_x 1
		.amdhsa_system_sgpr_workgroup_id_y 0
		.amdhsa_system_sgpr_workgroup_id_z 0
		.amdhsa_system_sgpr_workgroup_info 0
		.amdhsa_system_vgpr_workitem_id 0
		.amdhsa_next_free_vgpr 104
		.amdhsa_next_free_sgpr 91
		.amdhsa_accum_offset 104
		.amdhsa_reserve_vcc 1
		.amdhsa_float_round_mode_32 0
		.amdhsa_float_round_mode_16_64 0
		.amdhsa_float_denorm_mode_32 3
		.amdhsa_float_denorm_mode_16_64 3
		.amdhsa_dx10_clamp 1
		.amdhsa_ieee_mode 1
		.amdhsa_fp16_overflow 0
		.amdhsa_tg_split 0
		.amdhsa_exception_fp_ieee_invalid_op 0
		.amdhsa_exception_fp_denorm_src 0
		.amdhsa_exception_fp_ieee_div_zero 0
		.amdhsa_exception_fp_ieee_overflow 0
		.amdhsa_exception_fp_ieee_underflow 0
		.amdhsa_exception_fp_ieee_inexact 0
		.amdhsa_exception_int_div_zero 0
	.end_amdhsa_kernel

amdhsa.kernels:
  - .agpr_count:     0
    .args:
      - .actual_access:  write_only
        .address_space:  global
        .offset:         0
        .size:           8
        .value_kind:     global_buffer
      - .offset:         8
        .size:           4
        .value_kind:     by_value
      - .offset:         16
        .size:           4
        .value_kind:     hidden_block_count_x
      - .offset:         20
        .size:           4
        .value_kind:     hidden_block_count_y
      - .offset:         24
        .size:           4
        .value_kind:     hidden_block_count_z
      - .offset:         28
        .size:           2
        .value_kind:     hidden_group_size_x
      - .offset:         30
        .size:           2
        .value_kind:     hidden_group_size_y
      - .offset:         32
        .size:           2
        .value_kind:     hidden_group_size_z
      - .offset:         34
        .size:           2
        .value_kind:     hidden_remainder_x
      - .offset:         36
        .size:           2
        .value_kind:     hidden_remainder_y
      - .offset:         38
        .size:           2
        .value_kind:     hidden_remainder_z
      - .offset:         56
        .size:           8
        .value_kind:     hidden_global_offset_x
      - .offset:         64
        .size:           8
        .value_kind:     hidden_global_offset_y
      - .offset:         72
        .size:           8
        .value_kind:     hidden_global_offset_z
      - .offset:         80
        .size:           2
        .value_kind:     hidden_grid_dims
    .group_segment_fixed_size: 0
    .kernarg_segment_align: 8
    .kernarg_segment_size: 272
    .language:       OpenCL C
    .language_version:
      - 2
      - 0
    .max_flat_workgroup_size: 1024
    .name:           _Z11zero_kernelPDv4_fi
    .private_segment_fixed_size: 0
    .sgpr_count:     11
    .sgpr_spill_count: 0
    .symbol:         _Z11zero_kernelPDv4_fi.kd
    .uniform_work_group_size: 1
    .uses_dynamic_stack: false
    .vgpr_count:     6
    .vgpr_spill_count: 0
    .wavefront_size: 64
  - .agpr_count:     0
    .args:
      - .actual_access:  read_only
        .address_space:  global
        .offset:         0
        .size:           8
        .value_kind:     global_buffer
      - .actual_access:  read_only
        .address_space:  global
        .offset:         8
        .size:           8
        .value_kind:     global_buffer
      - .actual_access:  read_only
        .address_space:  global
        .offset:         16
        .size:           8
        .value_kind:     global_buffer
      - .actual_access:  read_only
        .address_space:  global
        .offset:         24
        .size:           8
        .value_kind:     global_buffer
      - .actual_access:  write_only
        .address_space:  global
        .offset:         32
        .size:           8
        .value_kind:     global_buffer
      - .actual_access:  read_only
        .address_space:  global
        .offset:         40
        .size:           8
        .value_kind:     global_buffer
      - .actual_access:  read_only
        .address_space:  global
        .offset:         48
        .size:           8
        .value_kind:     global_buffer
      - .address_space:  global
        .offset:         56
        .size:           8
        .value_kind:     global_buffer
      - .address_space:  global
        .offset:         64
        .size:           8
        .value_kind:     global_buffer
      - .address_space:  global
        .offset:         72
        .size:           8
        .value_kind:     global_buffer
      - .address_space:  global
        .offset:         80
        .size:           8
        .value_kind:     global_buffer
      - .offset:         88
        .size:           4
        .value_kind:     hidden_block_count_x
      - .offset:         92
        .size:           4
        .value_kind:     hidden_block_count_y
      - .offset:         96
        .size:           4
        .value_kind:     hidden_block_count_z
      - .offset:         100
        .size:           2
        .value_kind:     hidden_group_size_x
      - .offset:         102
        .size:           2
        .value_kind:     hidden_group_size_y
      - .offset:         104
        .size:           2
        .value_kind:     hidden_group_size_z
      - .offset:         106
        .size:           2
        .value_kind:     hidden_remainder_x
      - .offset:         108
        .size:           2
        .value_kind:     hidden_remainder_y
      - .offset:         110
        .size:           2
        .value_kind:     hidden_remainder_z
      - .offset:         128
        .size:           8
        .value_kind:     hidden_global_offset_x
      - .offset:         136
        .size:           8
        .value_kind:     hidden_global_offset_y
      - .offset:         144
        .size:           8
        .value_kind:     hidden_global_offset_z
      - .offset:         152
        .size:           2
        .value_kind:     hidden_grid_dims
    .group_segment_fixed_size: 61528
    .kernarg_segment_align: 8
    .kernarg_segment_size: 344
    .language:       OpenCL C
    .language_version:
      - 2
      - 0
    .max_flat_workgroup_size: 640
    .name:           _Z11p_gemm_mfmaPKfPKDv8_DF16_S0_S0_PDF16_PKiS6_PiS7_S7_S7_
    .private_segment_fixed_size: 0
    .sgpr_count:     36
    .sgpr_spill_count: 0
    .symbol:         _Z11p_gemm_mfmaPKfPKDv8_DF16_S0_S0_PDF16_PKiS6_PiS7_S7_S7_.kd
    .uniform_work_group_size: 1
    .uses_dynamic_stack: false
    .vgpr_count:     156
    .vgpr_spill_count: 0
    .wavefront_size: 64
  - .agpr_count:     0
    .args:
      - .actual_access:  read_only
        .address_space:  global
        .offset:         0
        .size:           8
        .value_kind:     global_buffer
      - .actual_access:  read_only
        .address_space:  global
        .offset:         8
        .size:           8
        .value_kind:     global_buffer
      - .actual_access:  read_only
        .address_space:  global
        .offset:         16
        .size:           8
        .value_kind:     global_buffer
      - .actual_access:  read_only
        .address_space:  global
        .offset:         24
        .size:           8
        .value_kind:     global_buffer
      - .actual_access:  read_only
        .address_space:  global
        .offset:         32
        .size:           8
        .value_kind:     global_buffer
      - .actual_access:  read_only
        .address_space:  global
        .offset:         40
        .size:           8
        .value_kind:     global_buffer
      - .actual_access:  read_only
        .address_space:  global
        .offset:         48
        .size:           8
        .value_kind:     global_buffer
      - .actual_access:  write_only
        .address_space:  global
        .offset:         56
        .size:           8
        .value_kind:     global_buffer
      - .actual_access:  write_only
        .address_space:  global
        .offset:         64
        .size:           8
        .value_kind:     global_buffer
      - .actual_access:  write_only
        .address_space:  global
        .offset:         72
        .size:           8
        .value_kind:     global_buffer
      - .actual_access:  write_only
        .address_space:  global
        .offset:         80
        .size:           8
        .value_kind:     global_buffer
      - .actual_access:  read_only
        .address_space:  global
        .offset:         88
        .size:           8
        .value_kind:     global_buffer
      - .actual_access:  write_only
        .address_space:  global
        .offset:         96
        .size:           8
        .value_kind:     global_buffer
      - .actual_access:  read_only
        .address_space:  global
        .offset:         104
        .size:           8
        .value_kind:     global_buffer
      - .actual_access:  read_only
        .address_space:  global
        .offset:         112
        .size:           8
        .value_kind:     global_buffer
      - .actual_access:  write_only
        .address_space:  global
        .offset:         120
        .size:           8
        .value_kind:     global_buffer
      - .actual_access:  read_only
        .address_space:  global
        .offset:         128
        .size:           8
        .value_kind:     global_buffer
      - .address_space:  global
        .offset:         136
        .size:           8
        .value_kind:     global_buffer
      - .address_space:  global
        .offset:         144
        .size:           8
        .value_kind:     global_buffer
      - .address_space:  global
        .offset:         152
        .size:           8
        .value_kind:     global_buffer
      - .address_space:  global
        .offset:         160
        .size:           8
        .value_kind:     global_buffer
      - .address_space:  global
        .offset:         168
        .size:           8
        .value_kind:     global_buffer
      - .offset:         176
        .size:           4
        .value_kind:     hidden_block_count_x
      - .offset:         180
        .size:           4
        .value_kind:     hidden_block_count_y
      - .offset:         184
        .size:           4
        .value_kind:     hidden_block_count_z
      - .offset:         188
        .size:           2
        .value_kind:     hidden_group_size_x
      - .offset:         190
        .size:           2
        .value_kind:     hidden_group_size_y
      - .offset:         192
        .size:           2
        .value_kind:     hidden_group_size_z
      - .offset:         194
        .size:           2
        .value_kind:     hidden_remainder_x
      - .offset:         196
        .size:           2
        .value_kind:     hidden_remainder_y
      - .offset:         198
        .size:           2
        .value_kind:     hidden_remainder_z
      - .offset:         216
        .size:           8
        .value_kind:     hidden_global_offset_x
      - .offset:         224
        .size:           8
        .value_kind:     hidden_global_offset_y
      - .offset:         232
        .size:           8
        .value_kind:     hidden_global_offset_z
      - .offset:         240
        .size:           2
        .value_kind:     hidden_grid_dims
    .group_segment_fixed_size: 1024
    .kernarg_segment_align: 8
    .kernarg_segment_size: 432
    .language:       OpenCL C
    .language_version:
      - 2
      - 0
    .max_flat_workgroup_size: 1024
    .name:           _Z12prep_weightsPKfS0_S0_S0_S0_S0_S0_PDF16_S1_S1_S1_S0_S1_S0_S0_PfPKiPiS5_S5_S5_S5_
    .private_segment_fixed_size: 0
    .sgpr_count:     48
    .sgpr_spill_count: 0
    .symbol:         _Z12prep_weightsPKfS0_S0_S0_S0_S0_S0_PDF16_S1_S1_S1_S0_S1_S0_S0_PfPKiPiS5_S5_S5_S5_.kd
    .uniform_work_group_size: 1
    .uses_dynamic_stack: false
    .vgpr_count:     29
    .vgpr_spill_count: 0
    .wavefront_size: 64
  - .agpr_count:     0
    .args:
      - .actual_access:  read_only
        .address_space:  global
        .offset:         0
        .size:           8
        .value_kind:     global_buffer
      - .actual_access:  read_only
        .address_space:  global
        .offset:         8
        .size:           8
        .value_kind:     global_buffer
      - .actual_access:  read_only
        .address_space:  global
        .offset:         16
        .size:           8
        .value_kind:     global_buffer
      - .actual_access:  read_only
        .address_space:  global
        .offset:         24
        .size:           8
        .value_kind:     global_buffer
      - .actual_access:  read_only
        .address_space:  global
        .offset:         32
        .size:           8
        .value_kind:     global_buffer
      - .actual_access:  read_only
        .address_space:  global
        .offset:         40
        .size:           8
        .value_kind:     global_buffer
      - .actual_access:  read_only
        .address_space:  global
        .offset:         48
        .size:           8
        .value_kind:     global_buffer
      - .actual_access:  read_only
        .address_space:  global
        .offset:         56
        .size:           8
        .value_kind:     global_buffer
      - .actual_access:  write_only
        .address_space:  global
        .offset:         64
        .size:           8
        .value_kind:     global_buffer
      - .actual_access:  read_only
        .address_space:  global
        .offset:         72
        .size:           8
        .value_kind:     global_buffer
      - .actual_access:  read_only
        .address_space:  global
        .offset:         80
        .size:           8
        .value_kind:     global_buffer
      - .actual_access:  read_only
        .address_space:  global
        .offset:         88
        .size:           8
        .value_kind:     global_buffer
      - .actual_access:  read_only
        .address_space:  global
        .offset:         96
        .size:           8
        .value_kind:     global_buffer
      - .actual_access:  read_only
        .address_space:  global
        .offset:         104
        .size:           8
        .value_kind:     global_buffer
    .group_segment_fixed_size: 160832
    .kernarg_segment_align: 8
    .kernarg_segment_size: 112
    .language:       OpenCL C
    .language_version:
      - 2
      - 0
    .max_flat_workgroup_size: 512
    .name:           _Z8gru_mfmaPKiPKDF16_PKDv8_DF16_S5_S5_S5_S0_S0_PfPKfS8_S8_S8_S0_
    .private_segment_fixed_size: 0
    .sgpr_count:     27
    .sgpr_spill_count: 0
    .symbol:         _Z8gru_mfmaPKiPKDF16_PKDv8_DF16_S5_S5_S5_S0_S0_PfPKfS8_S8_S8_S0_.kd
    .uniform_work_group_size: 1
    .uses_dynamic_stack: false
    .vgpr_count:     256
    .vgpr_spill_count: 0
    .wavefront_size: 64
  - .agpr_count:     0
    .args:
      - .actual_access:  read_only
        .address_space:  global
        .offset:         0
        .size:           8
        .value_kind:     global_buffer
      - .actual_access:  read_only
        .address_space:  global
        .offset:         8
        .size:           8
        .value_kind:     global_buffer
      - .actual_access:  read_only
        .address_space:  global
        .offset:         16
        .size:           8
        .value_kind:     global_buffer
      - .actual_access:  read_only
        .address_space:  global
        .offset:         24
        .size:           8
        .value_kind:     global_buffer
      - .actual_access:  read_only
        .address_space:  global
        .offset:         32
        .size:           8
        .value_kind:     global_buffer
      - .actual_access:  read_only
        .address_space:  global
        .offset:         40
        .size:           8
        .value_kind:     global_buffer
      - .actual_access:  read_only
        .address_space:  global
        .offset:         48
        .size:           8
        .value_kind:     global_buffer
      - .actual_access:  read_only
        .address_space:  global
        .offset:         56
        .size:           8
        .value_kind:     global_buffer
      - .actual_access:  write_only
        .address_space:  global
        .offset:         64
        .size:           8
        .value_kind:     global_buffer
    .group_segment_fixed_size: 26624
    .kernarg_segment_align: 8
    .kernarg_segment_size: 72
    .language:       OpenCL C
    .language_version:
      - 2
      - 0
    .max_flat_workgroup_size: 256
    .name:           _Z10gcn_kernelPKiS0_S0_S0_PKfS2_S2_S2_Pf
    .private_segment_fixed_size: 0
    .sgpr_count:     42
    .sgpr_spill_count: 0
    .symbol:         _Z10gcn_kernelPKiS0_S0_S0_PKfS2_S2_S2_Pf.kd
    .uniform_work_group_size: 1
    .uses_dynamic_stack: false
    .vgpr_count:     104
    .vgpr_spill_count: 0
    .wavefront_size: 64
